# flat-release barrier + pipelined polling: up to 3 staggered sc1 polls in flight into v255 (sampling period ~0.3us instead of one load round trip)
# speedup vs baseline: 1.0102x; 1.0005x over previous
.Lnb_poll_99:
	s_mov_b32 s10, 0
	s_nop 4
	global_load_dword v255, v1, s[8:9] sc1
	s_waitcnt vmcnt(0)
	v_sub_u32_e32 v3, v255, v2
	v_cmp_gt_i32_e32 vcc, 0, v3
	s_cbranch_vccz .Lnb_done_99
.Lnb_spin_99:
	global_load_dword v255, v1, s[8:9] sc1
	s_sleep 6
	s_waitcnt vmcnt(2)
	v_sub_u32_e32 v3, v255, v2
	v_cmp_gt_i32_e32 vcc, 0, v3
	s_cbranch_vccz .Lnb_done_99
	s_add_u32 s10, s10, 1
	s_cmp_lt_u32 s10, 0x80000
	s_cbranch_scc1 .Lnb_spin_99

.Lnb_poll_0:
	s_mov_b32 s14, 0
	s_nop 4
	global_load_dword v255, v3, s[6:7] sc1
	s_waitcnt vmcnt(0)
	v_sub_u32_e32 v2, v255, v1
	v_cmp_gt_i32_e32 vcc, 0, v2
	s_cbranch_vccz .Lnb_done_0
.Lnb_spin_0:
	global_load_dword v255, v3, s[6:7] sc1
	s_sleep 6
	s_waitcnt vmcnt(2)
	v_sub_u32_e32 v2, v255, v1
	v_cmp_gt_i32_e32 vcc, 0, v2
	s_cbranch_vccz .Lnb_done_0
	s_add_u32 s14, s14, 1
	s_cmp_lt_u32 s14, 0x80000
	s_cbranch_scc1 .Lnb_spin_0

	.amdhsa_kernel _Z8mega_fwd8MegaArgs
		.amdhsa_group_segment_fixed_size 0
		.amdhsa_private_segment_fixed_size 0
		.amdhsa_kernarg_size 432
		.amdhsa_user_sgpr_count 2
		.amdhsa_user_sgpr_dispatch_ptr 0
		.amdhsa_user_sgpr_queue_ptr 0
		.amdhsa_user_sgpr_kernarg_segment_ptr 1
		.amdhsa_user_sgpr_dispatch_id 0
		.amdhsa_user_sgpr_kernarg_preload_length 0
		.amdhsa_user_sgpr_kernarg_preload_offset 0
		.amdhsa_user_sgpr_private_segment_size 0
		.amdhsa_uses_dynamic_stack 0
		.amdhsa_enable_private_segment 0
		.amdhsa_system_sgpr_workgroup_id_x 1
		.amdhsa_system_sgpr_workgroup_id_y 0
		.amdhsa_system_sgpr_workgroup_id_z 0
		.amdhsa_system_sgpr_workgroup_info 0
		.amdhsa_system_vgpr_workitem_id 0
		.amdhsa_next_free_vgpr 256
		.amdhsa_next_free_sgpr 100
		.amdhsa_accum_offset 256
		.amdhsa_reserve_vcc 1
		.amdhsa_float_round_mode_32 0
		.amdhsa_float_round_mode_16_64 0
		.amdhsa_float_denorm_mode_32 3
		.amdhsa_float_denorm_mode_16_64 3
		.amdhsa_dx10_clamp 1
		.amdhsa_ieee_mode 1
		.amdhsa_fp16_overflow 0
		.amdhsa_tg_split 0
		.amdhsa_exception_fp_ieee_invalid_op 0
		.amdhsa_exception_fp_denorm_src 0
		.amdhsa_exception_fp_ieee_div_zero 0
		.amdhsa_exception_fp_ieee_overflow 0
		.amdhsa_exception_fp_ieee_underflow 0
		.amdhsa_exception_fp_ieee_inexact 0
		.amdhsa_exception_int_div_zero 0
	.end_amdhsa_kernel

amdhsa.kernels:
  - .agpr_count:     0
    .args:
      - .offset:         0
        .size:           176
        .value_kind:     by_value
      - .offset:         176
        .size:           4
        .value_kind:     hidden_block_count_x
      - .offset:         180
        .size:           4
        .value_kind:     hidden_block_count_y
      - .offset:         184
        .size:           4
        .value_kind:     hidden_block_count_z
      - .offset:         188
        .size:           2
        .value_kind:     hidden_group_size_x
      - .offset:         190
        .size:           2
        .value_kind:     hidden_group_size_y
      - .offset:         192
        .size:           2
        .value_kind:     hidden_group_size_z
      - .offset:         194
        .size:           2
        .value_kind:     hidden_remainder_x
      - .offset:         196
        .size:           2
        .value_kind:     hidden_remainder_y
      - .offset:         198
        .size:           2
        .value_kind:     hidden_remainder_z
      - .offset:         216
        .size:           8
        .value_kind:     hidden_global_offset_x
      - .offset:         224
        .size:           8
        .value_kind:     hidden_global_offset_y
      - .offset:         232
        .size:           8
        .value_kind:     hidden_global_offset_z
      - .offset:         240
        .size:           2
        .value_kind:     hidden_grid_dims
      - .offset:         296
        .size:           4
        .value_kind:     hidden_dynamic_lds_size
    .group_segment_fixed_size: 0
    .kernarg_segment_align: 8
    .kernarg_segment_size: 432
    .language:       OpenCL C
    .language_version:
      - 2
      - 0
    .max_flat_workgroup_size: 512
    .name:           _Z8mega_fwd8MegaArgs
    .private_segment_fixed_size: 0
    .sgpr_count:     106
    .sgpr_spill_count: 289
    .symbol:         _Z8mega_fwd8MegaArgs.kd
    .uniform_work_group_size: 1
    .uses_dynamic_stack: false
    .vgpr_count:     256
    .vgpr_spill_count: 0
    .wavefront_size: 64
